# speedup vs baseline: 1.0559x; 1.0066x over previous
_Z7k_fine3PKfS0_PKtS2_PKdS4_S0_PiPfS5_S0_S0_PtS7_:
	s_load_dwordx2 s[4:5], s[0:1], 0x30
	s_load_dwordx8 s[68:75], s[0:1], 0x0
	s_load_dwordx2 s[88:89], s[0:1], 0x48
	s_load_dwordx4 s[80:83], s[0:1], 0x20
	s_load_dwordx8 s[60:67], s[0:1], 0x50
	s_lshl_b32 s3, s2, 5
	s_and_b32 s3, s3, 0xe0
	s_lshr_b32 s76, s2, 3
	s_add_i32 s3, s3, s76
	s_lshr_b32 s84, s3, 1
	s_mov_b32 s85, 0
	s_lshl_b64 s[6:7], s[84:85], 14
	s_waitcnt lgkmcnt(0)
	s_add_u32 s4, s4, s6
	s_addc_u32 s5, s5, s7
	v_lshlrev_b32_e32 v2, 2, v0
	v_mov_b32_e32 v3, 0
	v_lshl_add_u64 v[4:5], s[4:5], 0, v[2:3]
	s_mov_b32 s6, 0x200000
	v_add_co_u32_e32 v6, vcc, s6, v4
	s_mov_b32 s7, 0x400000
	s_nop 0
	v_addc_co_u32_e32 v7, vcc, 0, v5, vcc
	v_or_b32_e32 v117, 0x400, v0
	v_add_co_u32_e32 v8, vcc, s7, v4
	v_lshlrev_b32_e32 v10, 2, v117
	v_mov_b32_e32 v11, v3
	v_addc_co_u32_e32 v9, vcc, 0, v5, vcc
	v_lshl_add_u64 v[12:13], s[4:5], 0, v[10:11]
	v_add_co_u32_e32 v14, vcc, s6, v12
	s_movk_i32 s8, 0x1000
	s_nop 0
	v_addc_co_u32_e32 v15, vcc, 0, v13, vcc
	v_add_co_u32_e32 v12, vcc, s7, v12
	v_or_b32_e32 v118, 0x800, v0
	s_nop 0
	v_addc_co_u32_e32 v13, vcc, 0, v13, vcc
	v_add_co_u32_e32 v16, vcc, s8, v4
	s_mov_b32 s8, 0x201000
	s_nop 0
	v_addc_co_u32_e32 v17, vcc, 0, v5, vcc
	v_add_co_u32_e32 v18, vcc, s8, v4
	s_mov_b32 s8, 0x401000
	s_nop 0
	v_addc_co_u32_e32 v19, vcc, 0, v5, vcc
	global_load_dword v24, v[6:7], off nt
	global_load_dword v25, v[8:9], off nt
	global_load_dword v26, v[8:9], off offset:2048 nt
	global_load_dword v27, v[14:15], off nt
	global_load_dword v28, v[12:13], off nt
	global_load_dword v29, v[16:17], off offset:2048 nt
	global_load_dword v30, v[18:19], off offset:2048 nt
	global_load_dword v31, v[6:7], off offset:2048 nt
	v_add_co_u32_e32 v6, vcc, s8, v4
	v_lshlrev_b32_e32 v8, 2, v118
	v_mov_b32_e32 v9, v3
	v_addc_co_u32_e32 v7, vcc, 0, v5, vcc
	v_lshl_add_u64 v[12:13], s[4:5], 0, v[8:9]
	global_load_dword v32, v2, s[4:5] nt
	global_load_dword v33, v2, s[4:5] offset:2048 nt
	global_load_dword v34, v10, s[4:5] nt
	global_load_dword v35, v8, s[4:5] nt
	v_add_co_u32_e32 v8, vcc, s6, v12
	s_movk_i32 s8, 0x2000
	s_nop 0
	v_addc_co_u32_e32 v9, vcc, 0, v13, vcc
	v_add_co_u32_e32 v10, vcc, s7, v12
	v_or_b32_e32 v1, 0xc00, v0
	s_nop 0
	v_addc_co_u32_e32 v11, vcc, 0, v13, vcc
	v_add_co_u32_e32 v12, vcc, s8, v4
	s_mov_b32 s8, 0x202000
	s_nop 0
	v_addc_co_u32_e32 v13, vcc, 0, v5, vcc
	v_add_co_u32_e32 v14, vcc, s8, v4
	s_mov_b32 s8, 0x402000
	s_nop 0
	v_addc_co_u32_e32 v15, vcc, 0, v5, vcc
	v_add_co_u32_e32 v16, vcc, s8, v4
	v_lshlrev_b32_e32 v18, 2, v1
	v_mov_b32_e32 v19, v3
	v_addc_co_u32_e32 v17, vcc, 0, v5, vcc
	v_lshl_add_u64 v[20:21], s[4:5], 0, v[18:19]
	v_add_co_u32_e32 v22, vcc, s6, v20
	s_movk_i32 s6, 0x3000
	s_nop 0
	v_addc_co_u32_e32 v23, vcc, 0, v21, vcc
	v_add_co_u32_e32 v20, vcc, s7, v20
	v_and_b32_e32 v124, 63, v0
	s_nop 0
	v_addc_co_u32_e32 v21, vcc, 0, v21, vcc
	global_load_dword v3, v[6:7], off offset:2048 nt
	global_load_dword v19, v[8:9], off nt
	global_load_dword v36, v[10:11], off nt
	global_load_dword v37, v[12:13], off offset:2048 nt
	global_load_dword v38, v[14:15], off offset:2048 nt
	global_load_dword v39, v[16:17], off offset:2048 nt
	global_load_dword v40, v[22:23], off nt
	global_load_dword v41, v[20:21], off nt
	v_add_co_u32_e32 v6, vcc, s6, v4
	s_mov_b32 s6, 0x203000
	s_nop 0
	v_addc_co_u32_e32 v7, vcc, 0, v5, vcc
	v_add_co_u32_e32 v8, vcc, s6, v4
	s_mov_b32 s6, 0x403000
	s_nop 0
	v_addc_co_u32_e32 v9, vcc, 0, v5, vcc
	v_add_co_u32_e32 v4, vcc, s6, v4
	v_lshrrev_b32_e32 v116, 6, v0
	s_nop 0
	v_addc_co_u32_e32 v5, vcc, 0, v5, vcc
	global_load_dword v13, v18, s[4:5] nt
	global_load_dword v14, v[6:7], off offset:2048 nt
	global_load_dword v15, v[8:9], off offset:2048 nt
	global_load_dword v16, v[4:5], off offset:2048 nt
	s_and_b32 s90, s84, 56
	s_lshl_b32 s91, s84, 3
	s_and_b32 s91, s91, 56
	s_or_b32 s90, s90, 4
	s_or_b32 s91, s91, 4
	s_lshr_b32 s92, s3, 7
	s_lshl_b32 s92, s92, 12
	v_lshrrev_b32_e32 v216, 5, v0
	v_mul_u32_u24_e32 v217, 57, v216
	v_lshrrev_b32_e32 v217, 9, v217
	v_mad_i32_i24 v216, v217, -9, v216
	v_add_u32_e32 v218, 1, v217
	v_mul_u32_u24_e32 v217, 0xab, v216
	v_lshrrev_b32_e32 v217, 9, v217
	v_mad_i32_i24 v216, v217, -3, v216
	v_add_u32_e32 v217, -1, v217
	v_add_u32_e32 v216, -1, v216
	v_mad_i32_i24 v217, v217, v218, s90
	v_mad_i32_i24 v216, v216, v218, s91
	v_lshl_add_u32 v217, v217, 6, v216
	v_add_u32_e32 v217, s92, v217
	v_and_b32_e32 v216, 31, v0
	v_lshlrev_b32_e32 v217, 9, v217
	v_lshl_add_u32 v217, v216, 4, v217
	global_load_dwordx4 v[220:223], v217, s[68:69]
	v_add_u32_e32 v219, 0x200, v0
	v_min_u32_e32 v219, 0x35f, v219
	v_lshrrev_b32_e32 v216, 5, v219
	v_mul_u32_u24_e32 v217, 57, v216
	v_lshrrev_b32_e32 v217, 9, v217
	v_mad_i32_i24 v216, v217, -9, v216
	v_add_u32_e32 v218, 1, v217
	v_mul_u32_u24_e32 v217, 0xab, v216
	v_lshrrev_b32_e32 v217, 9, v217
	v_mad_i32_i24 v216, v217, -3, v216
	v_add_u32_e32 v217, -1, v217
	v_add_u32_e32 v216, -1, v216
	v_mad_i32_i24 v217, v217, v218, s90
	v_mad_i32_i24 v216, v216, v218, s91
	v_lshl_add_u32 v217, v217, 6, v216
	v_add_u32_e32 v217, s92, v217
	v_and_b32_e32 v216, 31, v219
	v_lshlrev_b32_e32 v217, 9, v217
	v_lshl_add_u32 v217, v216, 4, v217
	global_load_dwordx4 v[224:227], v217, s[68:69]
	s_and_b32 s94, s76, 1
	s_lshl_b32 s94, s94, 2
	s_add_i32 s94, s94, s90
	s_add_i32 s94, s94, -5
	s_add_i32 s95, s91, -5
	v_mov_b32_e32 v250, v0
	v_lshrrev_b32_e32 v251, 5, v250
	v_and_b32_e32 v252, 31, v250
	v_mul_u32_u24_e32 v253, 0xcd, v251
	v_lshrrev_b32_e32 v253, 11, v253
	v_mad_i32_i24 v254, v253, -10, v251
	v_add_u32_e32 v253, s94, v253
	v_add_u32_e32 v254, s95, v254
	v_med3_i32 v253, v253, 0, 63
	v_med3_i32 v254, v254, 0, 63
	v_lshl_add_u32 v253, v253, 6, v254
	v_add_u32_e32 v253, s92, v253
	v_lshlrev_b32_e32 v253, 9, v253
	v_lshl_add_u32 v253, v252, 4, v253
	global_load_dwordx4 v[234:237], v253, s[68:69]
	v_add_u32_e32 v250, 0x200, v0
	v_lshrrev_b32_e32 v251, 5, v250
	v_and_b32_e32 v252, 31, v250
	v_mul_u32_u24_e32 v253, 0xcd, v251
	v_lshrrev_b32_e32 v253, 11, v253
	v_mad_i32_i24 v254, v253, -10, v251
	v_add_u32_e32 v253, s94, v253
	v_add_u32_e32 v254, s95, v254
	v_med3_i32 v253, v253, 0, 63
	v_med3_i32 v254, v254, 0, 63
	v_lshl_add_u32 v253, v253, 6, v254
	v_add_u32_e32 v253, s92, v253
	v_lshlrev_b32_e32 v253, 9, v253
	v_lshl_add_u32 v253, v252, 4, v253
	global_load_dwordx4 v[238:241], v253, s[68:69]
	v_add_u32_e32 v250, 0x400, v0
	v_lshrrev_b32_e32 v251, 5, v250
	v_and_b32_e32 v252, 31, v250
	v_mul_u32_u24_e32 v253, 0xcd, v251
	v_lshrrev_b32_e32 v253, 11, v253
	v_mad_i32_i24 v254, v253, -10, v251
	v_add_u32_e32 v253, s94, v253
	v_add_u32_e32 v254, s95, v254
	v_med3_i32 v253, v253, 0, 63
	v_med3_i32 v254, v254, 0, 63
	v_lshl_add_u32 v253, v253, 6, v254
	v_add_u32_e32 v253, s92, v253
	v_lshlrev_b32_e32 v253, 9, v253
	v_lshl_add_u32 v253, v252, 4, v253
	global_load_dwordx4 v[242:245], v253, s[68:69]
	v_add_u32_e32 v250, 0x600, v0
	v_min_u32_e32 v250, 0x77f, v250
	v_lshrrev_b32_e32 v251, 5, v250
	v_and_b32_e32 v252, 31, v250
	v_mul_u32_u24_e32 v253, 0xcd, v251
	v_lshrrev_b32_e32 v253, 11, v253
	v_mad_i32_i24 v254, v253, -10, v251
	v_add_u32_e32 v253, s94, v253
	v_add_u32_e32 v254, s95, v254
	v_med3_i32 v253, v253, 0, 63
	v_med3_i32 v254, v254, 0, 63
	v_lshl_add_u32 v253, v253, 6, v254
	v_add_u32_e32 v253, s92, v253
	v_lshlrev_b32_e32 v253, 9, v253
	v_lshl_add_u32 v253, v252, 4, v253
	global_load_dwordx4 v[246:249], v253, s[68:69]
	s_mov_b32 s4, 0xff800000
	v_cmp_eq_u32_e64 s[42:43], 0, v124
	s_waitcnt vmcnt(21)
	v_add_f32_e32 v4, v32, v24
	v_add_f32_e32 v12, v4, v25
	s_waitcnt vmcnt(20)
	v_add_f32_e32 v4, v33, v31
	s_waitcnt vmcnt(19)
	v_add_f32_e32 v5, v34, v27
	v_add_f32_e32 v11, v4, v26
	v_add_f32_e32 v10, v5, v28
	v_add_f32_e32 v5, v29, v30
	v_max3_f32 v4, v12, s4, v11
	s_waitcnt vmcnt(17)
	v_add_f32_e32 v9, v5, v3
	v_max3_f32 v3, v4, v10, v9
	s_waitcnt vmcnt(16)
	v_add_f32_e32 v4, v35, v19
	s_waitcnt vmcnt(15)
	v_add_f32_e32 v8, v4, v36
	s_waitcnt vmcnt(13)
	v_add_f32_e32 v4, v37, v38
	v_mbcnt_lo_u32_b32 v5, -1, 0
	s_waitcnt vmcnt(12)
	v_add_f32_e32 v7, v4, v39
	v_mbcnt_hi_u32_b32 v5, -1, v5
	v_max3_f32 v4, v3, v8, v7
	s_waitcnt vmcnt(9)
	v_add_f32_e32 v3, v13, v40
	v_and_b32_e32 v13, 64, v5
	v_add_f32_e32 v6, v3, v41
	s_waitcnt vmcnt(7)
	v_add_f32_e32 v3, v14, v15
	v_add_u32_e32 v13, 64, v13
	v_xor_b32_e32 v14, 1, v5
	v_cmp_lt_i32_e32 vcc, v14, v13
	s_waitcnt vmcnt(6)
	v_add_f32_e32 v3, v3, v16
	v_max3_f32 v4, v4, v6, v3
	v_cndmask_b32_e32 v14, v5, v14, vcc
	v_lshlrev_b32_e32 v115, 2, v14
	s_nop 1
	v_mov_b32_dpp v14, v4 quad_perm:[1,0,3,2] row_mask:0xf bank_mask:0xf
	s_waitcnt lgkmcnt(0)
	v_max_f32_e32 v14, v14, v14
	v_max_f32_e32 v4, v4, v14
	v_xor_b32_e32 v14, 2, v5
	v_cmp_lt_i32_e32 vcc, v14, v13
	s_nop 1
	v_cndmask_b32_e32 v14, v5, v14, vcc
	v_lshlrev_b32_e32 v114, 2, v14
	s_nop 1
	v_mov_b32_dpp v14, v4 quad_perm:[2,3,0,1] row_mask:0xf bank_mask:0xf
	s_waitcnt lgkmcnt(0)
	v_max_f32_e32 v14, v14, v14
	v_max_f32_e32 v4, v4, v14
	v_xor_b32_e32 v14, 4, v5
	v_cmp_lt_i32_e32 vcc, v14, v13
	s_nop 1
	v_cndmask_b32_e32 v14, v5, v14, vcc
	v_lshlrev_b32_e32 v113, 2, v14
	s_nop 1
	v_mov_b32_dpp v14, v4 row_half_mirror row_mask:0xf bank_mask:0xf
	s_waitcnt lgkmcnt(0)
	v_max_f32_e32 v14, v14, v14
	v_max_f32_e32 v4, v4, v14
	v_xor_b32_e32 v14, 8, v5
	v_cmp_lt_i32_e32 vcc, v14, v13
	s_nop 1
	v_cndmask_b32_e32 v14, v5, v14, vcc
	v_lshlrev_b32_e32 v112, 2, v14
	s_nop 1
	v_mov_b32_dpp v14, v4 row_mirror row_mask:0xf bank_mask:0xf
	s_waitcnt lgkmcnt(0)
	v_max_f32_e32 v14, v14, v14
	v_max_f32_e32 v4, v4, v14
	v_xor_b32_e32 v14, 16, v5
	v_cmp_lt_i32_e32 vcc, v14, v13
	s_nop 1
	v_cndmask_b32_e32 v14, v5, v14, vcc
	v_lshlrev_b32_e32 v122, 2, v14
	ds_bpermute_b32 v14, v122, v4
	s_waitcnt lgkmcnt(0)
	v_max_f32_e32 v14, v14, v14
	v_max_f32_e32 v4, v4, v14
	v_xor_b32_e32 v14, 32, v5
	v_cmp_lt_i32_e32 vcc, v14, v13
	s_nop 1
	v_cndmask_b32_e32 v5, v5, v14, vcc
	v_lshlrev_b32_e32 v121, 2, v5
	ds_bpermute_b32 v5, v121, v4
	s_and_saveexec_b64 s[4:5], s[42:43]
	s_cbranch_execz .LBB2_2
	s_waitcnt lgkmcnt(0)
	v_max_f32_e32 v5, v5, v5
	v_max_f32_e32 v4, v4, v4
	v_lshl_add_u32 v13, v116, 2, 0
	v_max_f32_e32 v4, v4, v5
	ds_write_b32 v13, v4 offset:65056
.LBB2_2:
	s_or_b64 exec, exec, s[4:5]
	v_cmp_eq_u32_e32 vcc, 0, v0
	s_and_saveexec_b64 s[4:5], vcc
	v_mov_b32_e32 v4, 0
	ds_write_b32 v4, v4 offset:65088
	s_or_b64 exec, exec, s[4:5]
	s_lshl_b32 s4, s84, 3
	s_and_b32 s77, s84, 56
	s_and_b32 s33, s4, 56
	s_movk_i32 s4, 0x360
	s_lshr_b32 s86, s3, 7
	s_or_b32 s10, s77, 4
	s_or_b32 s11, s33, 4
	s_mov_b32 s87, 0
	s_lshl_b64 s[6:7], s[86:87], 12
	s_mov_b64 s[8:9], 0
	s_movk_i32 s12, 0xab
	s_movk_i32 s13, 0x15f
	v_lshlrev_b32_e32 v228, 4, v0
	s_waitcnt vmcnt(5) lgkmcnt(0)
	ds_write_b128 v228, v[220:223]
	s_movk_i32 s4, 0x160
	v_cmp_gt_u32_e32 vcc, s4, v0
	s_and_saveexec_b64 s[4:5], vcc
	s_waitcnt vmcnt(4)
	ds_write_b128 v228, v[224:227] offset:8192
	s_or_b64 exec, exec, s[4:5]
	s_waitcnt vmcnt(0)
	v_mov_b32_e32 v250, v0
	v_lshrrev_b32_e32 v251, 5, v250
	v_and_b32_e32 v252, 31, v250
	v_lshlrev_b32_e32 v251, 9, v251
	v_and_b32_e32 v253, 1, v252
	v_lshrrev_b32_e32 v252, 1, v252
	v_lshl_add_u32 v251, v253, 8, v251
	v_lshl_add_u32 v251, v252, 4, v251
	v_add_u32_e32 v251, 0x13e00, v251
	ds_write_b128 v251, v[234:237]
	v_add_u32_e32 v250, 0x200, v0
	v_lshrrev_b32_e32 v251, 5, v250
	v_and_b32_e32 v252, 31, v250
	v_lshlrev_b32_e32 v251, 9, v251
	v_and_b32_e32 v253, 1, v252
	v_lshrrev_b32_e32 v252, 1, v252
	v_lshl_add_u32 v251, v253, 8, v251
	v_lshl_add_u32 v251, v252, 4, v251
	v_add_u32_e32 v251, 0x13e00, v251
	ds_write_b128 v251, v[238:241]
	v_add_u32_e32 v250, 0x400, v0
	v_lshrrev_b32_e32 v251, 5, v250
	v_and_b32_e32 v252, 31, v250
	v_lshlrev_b32_e32 v251, 9, v251
	v_and_b32_e32 v253, 1, v252
	v_lshrrev_b32_e32 v252, 1, v252
	v_lshl_add_u32 v251, v253, 8, v251
	v_lshl_add_u32 v251, v252, 4, v251
	v_add_u32_e32 v251, 0x13e00, v251
	ds_write_b128 v251, v[242:245]
	v_add_u32_e32 v250, 0x600, v0
	v_lshrrev_b32_e32 v251, 5, v250
	v_and_b32_e32 v252, 31, v250
	v_lshlrev_b32_e32 v251, 9, v251
	v_and_b32_e32 v253, 1, v252
	v_lshrrev_b32_e32 v252, 1, v252
	v_lshl_add_u32 v251, v253, 8, v251
	v_lshl_add_u32 v251, v252, 4, v251
	v_add_u32_e32 v251, 0x13e00, v251
	v_cmp_gt_u32_e32 vcc, 0x180, v0
	s_and_saveexec_b64 s[98:99], vcc
	ds_write_b128 v251, v[246:249]
	s_or_b64 exec, exec, s[98:99]
	s_load_dwordx4 s[4:7], s[0:1], 0x38
	v_subrev_u32_e32 v2, 64, v0
	v_cmp_gt_u32_e32 vcc, 3, v2
	v_lshl_add_u32 v119, v0, 3, 0
	s_waitcnt lgkmcnt(0)
	v_writelane_b32 v212, s4, 0
	s_nop 1
	v_writelane_b32 v212, s5, 1
	v_writelane_b32 v212, s6, 2
	v_writelane_b32 v212, s7, 3
	s_and_saveexec_b64 s[0:1], vcc
	s_cbranch_execz .LBB2_9
	s_lshl_b32 s4, s86, 12
	s_or_b32 s6, s11, s4
	v_sub_u32_e32 v5, 63, v0
	v_add_lshl_u32 v4, s10, v5, 6
	v_add_u32_e32 v13, s6, v5
	v_or_b32_e32 v14, v13, v4
	v_mov_b32_e32 v15, 0
	s_or_b32 s7, s33, s4
	v_subrev_u32_e32 v2, 63, v0
	v_lshl_add_u64 v[16:17], v[14:15], 3, s[80:81]
	v_add_u32_e32 v14, s7, v4
	v_mov_b32_e32 v5, v15
	v_lshl_add_u64 v[18:19], v[14:15], 3, s[80:81]
	v_add_u32_e32 v14, s7, v2
	s_lshl_b32 s4, s10, 6
	v_lshl_add_u64 v[4:5], v[14:15], 0, v[4:5]
	v_or_b32_e32 v20, s4, v13
	v_mov_b32_e32 v21, v15
	s_mov_b32 s5, 0
	v_lshl_add_u64 v[4:5], v[4:5], 3, s[80:81]
	v_lshl_add_u64 v[20:21], v[20:21], 3, s[80:81]
	global_load_dwordx2 v[22:23], v[16:17], off
	global_load_dwordx2 v[24:25], v[18:19], off offset:32
	global_load_dwordx2 v[26:27], v[4:5], off offset:32
	global_load_dwordx2 v[28:29], v[20:21], off
	v_add_lshl_u32 v16, s10, v2, 6
	v_lshl_add_u64 v[4:5], v[14:15], 0, s[4:5]
	v_add_u32_e32 v14, v13, v16
	v_add_u32_e32 v16, s6, v16
	v_lshl_add_u64 v[4:5], v[4:5], 3, s[80:81]
	v_ashrrev_i32_e32 v15, 31, v14
	v_ashrrev_i32_e32 v17, 31, v16
	v_lshl_add_u64 v[14:15], v[14:15], 3, s[80:81]
	v_lshl_add_u64 v[18:19], v[16:17], 3, s[80:81]
	global_load_dwordx2 v[20:21], v[4:5], off offset:32
	global_load_dwordx2 v[30:31], v[14:15], off
	global_load_dwordx2 v[32:33], v[18:19], off
	v_add_u32_e32 v4, v16, v2
	v_ashrrev_i32_e32 v5, 31, v4
	v_lshl_add_u64 v[4:5], v[4:5], 3, s[80:81]
	global_load_dwordx2 v[4:5], v[4:5], off
	s_or_b32 s4, s7, s4
	s_lshl_b64 s[4:5], s[4:5], 3
	s_add_u32 s4, s80, s4
	s_addc_u32 s5, s81, s5
	s_load_dwordx2 s[4:5], s[4:5], 0x20
	s_mov_b32 s6, 0
	s_brev_b32 s7, 8
	v_mov_b32_e32 v2, 0x100
	v_mov_b32_e32 v13, 0xffffff80
	v_mov_b32_e32 v34, 0x260
	s_waitcnt vmcnt(7)
	v_add_f64 v[14:15], v[22:23], 0
	s_waitcnt vmcnt(6)
	v_add_f64 v[14:15], v[14:15], v[24:25]
	s_waitcnt vmcnt(5)
	v_add_f64 v[14:15], v[14:15], v[26:27]
	s_waitcnt vmcnt(4)
	v_add_f64 v[14:15], v[14:15], v[28:29]
	s_waitcnt lgkmcnt(0)
	v_add_f64 v[14:15], v[14:15], s[4:5]
	s_mov_b32 s4, 0x812dea11
	s_mov_b32 s5, 0x3d719799
	s_waitcnt vmcnt(3)
	v_add_f64 v[14:15], v[14:15], v[20:21]
	s_waitcnt vmcnt(2)
	v_add_f64 v[14:15], v[14:15], v[30:31]
	s_waitcnt vmcnt(1)
	v_add_f64 v[14:15], v[14:15], v[32:33]
	s_waitcnt vmcnt(0)
	v_add_f64 v[4:5], v[14:15], v[4:5]
	v_cmp_gt_f64_e32 vcc, s[6:7], v[4:5]
	s_nop 1
	v_cndmask_b32_e32 v2, 0, v2, vcc
	v_ldexp_f64 v[4:5], v[4:5], v2
	v_rsq_f64_e32 v[14:15], v[4:5]
	v_cndmask_b32_e32 v2, 0, v13, vcc
	v_cmp_class_f64_e32 vcc, v[4:5], v34
	v_mul_f64 v[16:17], v[4:5], v[14:15]
	v_mul_f64 v[14:15], v[14:15], 0.5
	v_fma_f64 v[18:19], -v[14:15], v[16:17], 0.5
	v_fmac_f64_e32 v[16:17], v[16:17], v[18:19]
	v_fmac_f64_e32 v[14:15], v[14:15], v[18:19]
	v_fma_f64 v[18:19], -v[16:17], v[16:17], v[4:5]
	v_fmac_f64_e32 v[16:17], v[18:19], v[14:15]
	v_fma_f64 v[18:19], -v[16:17], v[16:17], v[4:5]
	v_fmac_f64_e32 v[16:17], v[18:19], v[14:15]
	v_ldexp_f64 v[14:15], v[16:17], v2
	v_cndmask_b32_e32 v5, v15, v5, vcc
	v_cndmask_b32_e32 v4, v14, v4, vcc
	v_max_f64 v[4:5], v[4:5], s[4:5]
	v_div_scale_f64 v[14:15], s[4:5], v[4:5], v[4:5], 1.0
	v_rcp_f64_e32 v[16:17], v[14:15]
	v_div_scale_f64 v[18:19], vcc, 1.0, v[4:5], 1.0
	v_fma_f64 v[20:21], -v[14:15], v[16:17], 1.0
	v_fmac_f64_e32 v[16:17], v[16:17], v[20:21]
	v_fma_f64 v[20:21], -v[14:15], v[16:17], 1.0
	v_fmac_f64_e32 v[16:17], v[16:17], v[20:21]
	v_mul_f64 v[20:21], v[18:19], v[16:17]
	v_fma_f64 v[14:15], -v[14:15], v[20:21], v[18:19]
	v_div_fmas_f64 v[14:15], v[14:15], v[16:17], v[20:21]
	v_div_fixup_f64 v[4:5], v[14:15], v[4:5], 1.0
	ds_write_b64 v119, v[4:5] offset:64512

.LBB2_110:
	s_or_b64 exec, exec, s[0:1]
	v_bfe_u32 v65, v0, 6, 1
	v_bfe_u32 v1, v0, 3, 1
	v_lshl_or_b32 v46, v65, 1, v1
	v_lshrrev_b32_e32 v1, 3, v0
	v_and_b32_e32 v97, 15, v0
	v_and_b32_e32 v1, 48, v1
	v_or_b32_e32 v63, v1, v97
	v_mul_lo_u16_e32 v2, 20, v63
	v_lshrrev_b16_e32 v2, 7, v2
	v_and_b32_e32 v2, 14, v2
	v_or_b32_e32 v110, 64, v63
	v_add_u32_sdwa v6, v63, v2 dst_sel:DWORD dst_unused:UNUSED_PAD src0_sel:DWORD src1_sel:WORD_0
	v_mul_lo_u16_e32 v2, 0x4f, v110
	v_lshrrev_b16_e32 v2, 9, v2
	v_and_b32_e32 v2, 62, v2
	v_bfe_u32 v62, v0, 4, 2
	v_and_b32_e32 v47, 7, v0
	v_add_u32_e32 v10, v110, v2
	v_lshl_add_u32 v84, v62, 4, 0
	v_mad_u32_u24 v2, v46, 10, v47
	s_movk_i32 s0, 0x110
	s_waitcnt vmcnt(4)
	v_mad_u32_u24 v34, v2, s0, v84
	s_waitcnt lgkmcnt(0)
	s_barrier
	ds_read_b128 v[2:5], v34 offset:61200
	v_or_b32_e32 v64, 0x80, v63
	v_min_u32_e32 v22, 0xa8, v64
	v_mul_lo_u16_e32 v7, 0x4f, v22
	v_lshrrev_b32_e32 v180, 4, v1
	v_lshrrev_b32_e32 v181, 1, v180
	v_and_b32_e32 v182, 1, v180
	v_lshl_or_b32 v181, v181, 5, v182
	v_add_u32_e32 v183, 4, v97
	v_add_u32_e32 v184, -8, v97
	v_cmp_gt_u32_e64 s[90:91], 4, v97
	v_cmp_lt_u32_e64 s[92:93], 11, v97
	v_mov_b32_e32 v188, 0xc0
	s_nop 0
	v_cndmask_b32_e64 v183, v183, v97, s[90:91]
	v_cndmask_b32_e64 v183, v183, v184, s[92:93]
	v_lshl_add_u32 v185, v183, 1, v181
	v_add_u32_e32 v186, 64, v185
	v_add_u32_e32 v187, 0x80, v185
	v_cmp_eq_u32_e32 vcc, 0xa4, v187
	s_nop 1
	v_cndmask_b32_e32 v187, v187, v188, vcc
	v_mul_u32_u24_e32 v189, 0x89, v185
	v_lshrrev_b32_e32 v189, 11, v189
	v_mad_i32_i24 v190, v189, -15, v185
	v_cmp_gt_u32_e32 vcc, 13, v190
	v_lshlrev_b32_e32 v191, 1, v189
	v_sub_u32_e32 v193, v185, v191
	v_mad_u32_u24 v98, v185, s0, v84
	v_cndmask_b32_e64 v196, 0, 1, vcc
	v_mul_u32_u24_e32 v189, 0x89, v186
	v_lshrrev_b32_e32 v189, 11, v189
	v_mad_i32_i24 v190, v189, -15, v186
	v_cmp_gt_u32_e32 vcc, 13, v190
	v_lshlrev_b32_e32 v191, 1, v189
	v_sub_u32_e32 v194, v186, v191
	v_mad_u32_u24 v111, v186, s0, v84
	v_cndmask_b32_e64 v197, 0, 1, vcc
	v_mul_u32_u24_e32 v189, 0x89, v187
	v_lshrrev_b32_e32 v189, 11, v189
	v_mad_i32_i24 v190, v189, -15, v187
	v_cmp_gt_u32_e32 vcc, 13, v190
	v_lshlrev_b32_e32 v191, 1, v189
	v_sub_u32_e32 v195, v187, v191
	v_mad_u32_u24 v117, v187, s0, v84
	v_cndmask_b32_e64 v198, 0, 1, vcc
	v_lshrrev_b16_e32 v23, 9, v7
	ds_read_b128 v[6:9], v98
	ds_read_b128 v[10:13], v111
	ds_read_b128 v[14:17], v34 offset:61264
	ds_read_b128 v[18:21], v98 offset:64
	v_and_b32_e32 v23, 30, v23
	s_waitcnt lgkmcnt(3)
	v_mfma_f32_16x16x32_f16 v[6:9], v[2:5], v[6:9], 0
	v_add_u32_e32 v26, v22, v23
	ds_read_b128 v[22:25], v111 offset:64
	ds_read_b128 v[26:29], v117
	ds_read_b128 v[30:33], v117 offset:64
	s_waitcnt lgkmcnt(3)
	v_mfma_f32_16x16x32_f16 v[6:9], v[14:17], v[18:21], v[6:9]
	ds_read_b128 v[18:21], v34 offset:61328
	v_add_u32_e32 v58, 1, v47
	v_add_u32_e32 v85, 2, v47
	v_mfma_f32_16x16x32_f16 v[10:13], v[2:5], v[10:13], 0
	v_lshl_or_b32 v86, s2, 9, v0
	v_ashrrev_i32_e32 v87, 31, v86
	v_lshlrev_b64 v[74:75], 4, v[86:87]
	s_waitcnt lgkmcnt(2)
	v_mfma_f32_16x16x32_f16 v[2:5], v[2:5], v[26:29], 0
	v_mad_u32_u24 v90, v46, 10, 20
	v_lshl_add_u64 v[70:71], s[60:61], 0, v[74:75]
	v_add_co_u32_e32 v42, vcc, 0x200000, v70
	v_mfma_f32_16x16x32_f16 v[10:13], v[14:17], v[22:25], v[10:13]
	s_nop 0
	v_addc_co_u32_e32 v43, vcc, 0, v71, vcc
	v_add_co_u32_e32 v50, vcc, 0x400000, v70
	s_waitcnt lgkmcnt(1)
	v_mfma_f32_16x16x32_f16 v[2:5], v[14:17], v[30:33], v[2:5]
	ds_read_b128 v[14:17], v98 offset:128
	ds_read_b128 v[22:25], v34 offset:61392
	ds_read_b128 v[26:29], v98 offset:192
	v_addc_co_u32_e32 v51, vcc, 0, v71, vcc
	s_waitcnt lgkmcnt(2)
	v_mfma_f32_16x16x32_f16 v[6:9], v[18:21], v[14:17], v[6:9]
	ds_read_b128 v[14:17], v111 offset:128
	ds_read_b128 v[30:33], v111 offset:192
	v_add_co_u32_e32 v52, vcc, 0x600000, v70
	s_waitcnt lgkmcnt(1)
	v_mfma_f32_16x16x32_f16 v[10:13], v[18:21], v[14:17], v[10:13]
	ds_read_b128 v[14:17], v117 offset:128
	ds_read_b128 v[34:37], v117 offset:192
	v_addc_co_u32_e32 v53, vcc, 0, v71, vcc
	s_waitcnt lgkmcnt(1)
	v_mfma_f32_16x16x32_f16 v[2:5], v[18:21], v[14:17], v[2:5]
	v_mad_u32_u24 v14, v46, 10, v58
	v_mad_u32_u24 v38, v14, s0, v84
	ds_read_b128 v[14:17], v38 offset:61200
	v_mfma_f32_16x16x32_f16 v[6:9], v[22:25], v[26:29], v[6:9]
	v_add_co_u32_e32 v54, vcc, 0x800000, v70
	s_mov_b32 s1, 0x200000
	v_mfma_f32_16x16x32_f16 v[10:13], v[22:25], v[30:33], v[10:13]
	v_addc_co_u32_e32 v55, vcc, 0, v71, vcc
	v_lshl_add_u64 v[82:83], s[62:63], 0, v[74:75]
	s_waitcnt lgkmcnt(1)
	v_mfma_f32_16x16x32_f16 v[2:5], v[22:25], v[34:37], v[2:5]
	ds_read_b128 v[18:21], v98 offset:272
	ds_read_b128 v[22:25], v38 offset:61264
	ds_read_b128 v[26:29], v98 offset:336
	s_mov_b32 s2, 0x400000
	s_mov_b32 s3, 0x600000
	s_waitcnt lgkmcnt(2)
	v_mfma_f32_16x16x32_f16 v[6:9], v[14:17], v[18:21], v[6:9]
	ds_read_b128 v[18:21], v111 offset:272
	ds_read_b128 v[30:33], v111 offset:336
	s_add_i32 s6, 0, 0x13890
	s_waitcnt lgkmcnt(1)
	v_mfma_f32_16x16x32_f16 v[10:13], v[14:17], v[18:21], v[10:13]
	ds_read_b128 v[18:21], v117 offset:272
	ds_read_b128 v[34:37], v117 offset:336
	s_waitcnt lgkmcnt(1)
	v_mfma_f32_16x16x32_f16 v[2:5], v[14:17], v[18:21], v[2:5]
	ds_read_b128 v[14:17], v38 offset:61328
	v_mfma_f32_16x16x32_f16 v[6:9], v[22:25], v[26:29], v[6:9]
	v_mfma_f32_16x16x32_f16 v[10:13], v[22:25], v[30:33], v[10:13]
	s_waitcnt lgkmcnt(1)
	v_mfma_f32_16x16x32_f16 v[2:5], v[22:25], v[34:37], v[2:5]
	ds_read_b128 v[18:21], v98 offset:400
	ds_read_b128 v[22:25], v38 offset:61392
	ds_read_b128 v[26:29], v98 offset:464
	s_waitcnt lgkmcnt(2)
	v_mfma_f32_16x16x32_f16 v[6:9], v[14:17], v[18:21], v[6:9]
	ds_read_b128 v[18:21], v111 offset:400
	ds_read_b128 v[30:33], v111 offset:464
	s_waitcnt lgkmcnt(1)
	v_mfma_f32_16x16x32_f16 v[10:13], v[14:17], v[18:21], v[10:13]
	ds_read_b128 v[18:21], v117 offset:400
	ds_read_b128 v[34:37], v117 offset:464
	s_waitcnt lgkmcnt(1)
	v_mfma_f32_16x16x32_f16 v[2:5], v[14:17], v[18:21], v[2:5]
	v_mad_u32_u24 v14, v46, 10, v85
	v_mad_u32_u24 v38, v14, s0, v84
	ds_read_b128 v[14:17], v38 offset:61200
	v_mfma_f32_16x16x32_f16 v[6:9], v[22:25], v[26:29], v[6:9]
	v_mfma_f32_16x16x32_f16 v[10:13], v[22:25], v[30:33], v[10:13]
	s_waitcnt lgkmcnt(1)
	v_mfma_f32_16x16x32_f16 v[2:5], v[22:25], v[34:37], v[2:5]
	ds_read_b128 v[18:21], v98 offset:544
	ds_read_b128 v[22:25], v38 offset:61264
	ds_read_b128 v[26:29], v98 offset:608
	s_waitcnt lgkmcnt(2)
	v_mfma_f32_16x16x32_f16 v[6:9], v[14:17], v[18:21], v[6:9]
	ds_read_b128 v[18:21], v111 offset:544
	ds_read_b128 v[30:33], v111 offset:608
	s_waitcnt lgkmcnt(1)
	v_mfma_f32_16x16x32_f16 v[10:13], v[14:17], v[18:21], v[10:13]
	ds_read_b128 v[18:21], v117 offset:544
	ds_read_b128 v[34:37], v117 offset:608
	s_waitcnt lgkmcnt(1)
	v_mfma_f32_16x16x32_f16 v[2:5], v[14:17], v[18:21], v[2:5]
	ds_read_b128 v[14:17], v38 offset:61328
	v_mfma_f32_16x16x32_f16 v[6:9], v[22:25], v[26:29], v[6:9]
	v_mfma_f32_16x16x32_f16 v[10:13], v[22:25], v[30:33], v[10:13]
	s_waitcnt lgkmcnt(1)
	v_mfma_f32_16x16x32_f16 v[2:5], v[22:25], v[34:37], v[2:5]
	ds_read_b128 v[18:21], v98 offset:672
	ds_read_b128 v[22:25], v38 offset:61392
	ds_read_b128 v[26:29], v98 offset:736
	v_mad_u32_u24 v38, v46, 10, 10
	s_waitcnt lgkmcnt(2)
	v_mfma_f32_16x16x32_f16 v[6:9], v[14:17], v[18:21], v[6:9]
	ds_read_b128 v[18:21], v111 offset:672
	ds_read_b128 v[30:33], v111 offset:736
	s_waitcnt lgkmcnt(1)
	v_mfma_f32_16x16x32_f16 v[10:13], v[14:17], v[18:21], v[10:13]
	ds_read_b128 v[18:21], v117 offset:672
	ds_read_b128 v[34:37], v117 offset:736
	s_waitcnt lgkmcnt(1)
	v_mfma_f32_16x16x32_f16 v[2:5], v[14:17], v[18:21], v[2:5]
	v_add_u32_e32 v14, v47, v38
	v_mad_u32_u24 v39, v14, s0, v84
	ds_read_b128 v[14:17], v39 offset:61200
	v_mfma_f32_16x16x32_f16 v[6:9], v[22:25], v[26:29], v[6:9]
	v_mfma_f32_16x16x32_f16 v[10:13], v[22:25], v[30:33], v[10:13]
	s_waitcnt lgkmcnt(1)
	v_mfma_f32_16x16x32_f16 v[2:5], v[22:25], v[34:37], v[2:5]
	ds_read_b128 v[18:21], v98 offset:4080
	ds_read_b128 v[22:25], v39 offset:61264
	ds_read_b128 v[26:29], v98 offset:4144
	s_waitcnt lgkmcnt(2)
	v_mfma_f32_16x16x32_f16 v[6:9], v[14:17], v[18:21], v[6:9]
	ds_read_b128 v[18:21], v111 offset:4080
	ds_read_b128 v[30:33], v111 offset:4144
	s_waitcnt lgkmcnt(1)
	v_mfma_f32_16x16x32_f16 v[10:13], v[14:17], v[18:21], v[10:13]
	ds_read_b128 v[18:21], v117 offset:4080
	ds_read_b128 v[34:37], v117 offset:4144
	s_waitcnt lgkmcnt(1)
	v_mfma_f32_16x16x32_f16 v[2:5], v[14:17], v[18:21], v[2:5]
	ds_read_b128 v[14:17], v39 offset:61328
	v_mfma_f32_16x16x32_f16 v[6:9], v[22:25], v[26:29], v[6:9]
	v_mfma_f32_16x16x32_f16 v[10:13], v[22:25], v[30:33], v[10:13]
	s_waitcnt lgkmcnt(1)
	v_mfma_f32_16x16x32_f16 v[2:5], v[22:25], v[34:37], v[2:5]
	ds_read_b128 v[18:21], v98 offset:4208
	ds_read_b128 v[22:25], v39 offset:61392
	ds_read_b128 v[26:29], v98 offset:4272
	s_waitcnt lgkmcnt(2)
	v_mfma_f32_16x16x32_f16 v[6:9], v[14:17], v[18:21], v[6:9]
	ds_read_b128 v[18:21], v111 offset:4208
	ds_read_b128 v[30:33], v111 offset:4272
	s_waitcnt lgkmcnt(1)
	v_mfma_f32_16x16x32_f16 v[10:13], v[14:17], v[18:21], v[10:13]
	ds_read_b128 v[18:21], v117 offset:4208
	ds_read_b128 v[34:37], v117 offset:4272
	s_waitcnt lgkmcnt(1)
	v_mfma_f32_16x16x32_f16 v[2:5], v[14:17], v[18:21], v[2:5]
	v_add_u32_e32 v14, v58, v38
	v_mad_u32_u24 v39, v14, s0, v84
	ds_read_b128 v[14:17], v39 offset:61200
	v_mfma_f32_16x16x32_f16 v[6:9], v[22:25], v[26:29], v[6:9]
	v_mfma_f32_16x16x32_f16 v[10:13], v[22:25], v[30:33], v[10:13]
	s_waitcnt lgkmcnt(1)
	v_mfma_f32_16x16x32_f16 v[2:5], v[22:25], v[34:37], v[2:5]
	ds_read_b128 v[18:21], v98 offset:4352
	ds_read_b128 v[22:25], v39 offset:61264
	ds_read_b128 v[26:29], v98 offset:4416
	s_waitcnt lgkmcnt(2)
	v_mfma_f32_16x16x32_f16 v[6:9], v[14:17], v[18:21], v[6:9]
	ds_read_b128 v[18:21], v111 offset:4352
	ds_read_b128 v[30:33], v111 offset:4416
	s_waitcnt lgkmcnt(1)
	v_mfma_f32_16x16x32_f16 v[10:13], v[14:17], v[18:21], v[10:13]
	ds_read_b128 v[18:21], v117 offset:4352
	ds_read_b128 v[34:37], v117 offset:4416
	s_waitcnt lgkmcnt(1)
	v_mfma_f32_16x16x32_f16 v[2:5], v[14:17], v[18:21], v[2:5]
	ds_read_b128 v[14:17], v39 offset:61328
	v_mfma_f32_16x16x32_f16 v[6:9], v[22:25], v[26:29], v[6:9]
	v_mfma_f32_16x16x32_f16 v[10:13], v[22:25], v[30:33], v[10:13]
	s_waitcnt lgkmcnt(1)
	v_mfma_f32_16x16x32_f16 v[2:5], v[22:25], v[34:37], v[2:5]
	ds_read_b128 v[18:21], v98 offset:4480
	ds_read_b128 v[22:25], v39 offset:61392
	ds_read_b128 v[26:29], v98 offset:4544
	s_waitcnt lgkmcnt(2)
	v_mfma_f32_16x16x32_f16 v[6:9], v[14:17], v[18:21], v[6:9]
	ds_read_b128 v[18:21], v111 offset:4480
	ds_read_b128 v[30:33], v111 offset:4544
	s_waitcnt lgkmcnt(1)
	v_mfma_f32_16x16x32_f16 v[10:13], v[14:17], v[18:21], v[10:13]
	ds_read_b128 v[18:21], v117 offset:4480
	ds_read_b128 v[34:37], v117 offset:4544
	s_waitcnt lgkmcnt(1)
	v_mfma_f32_16x16x32_f16 v[2:5], v[14:17], v[18:21], v[2:5]
	v_add_u32_e32 v14, v85, v38
	v_mad_u32_u24 v38, v14, s0, v84
	ds_read_b128 v[14:17], v38 offset:61200
	v_mfma_f32_16x16x32_f16 v[6:9], v[22:25], v[26:29], v[6:9]
	v_mfma_f32_16x16x32_f16 v[10:13], v[22:25], v[30:33], v[10:13]
	s_waitcnt lgkmcnt(1)
	v_mfma_f32_16x16x32_f16 v[2:5], v[22:25], v[34:37], v[2:5]
	ds_read_b128 v[18:21], v98 offset:4624
	ds_read_b128 v[22:25], v38 offset:61264
	ds_read_b128 v[26:29], v98 offset:4688
	s_waitcnt lgkmcnt(2)
	v_mfma_f32_16x16x32_f16 v[6:9], v[14:17], v[18:21], v[6:9]
	ds_read_b128 v[18:21], v111 offset:4624
	ds_read_b128 v[30:33], v111 offset:4688
	s_waitcnt lgkmcnt(1)
	v_mfma_f32_16x16x32_f16 v[10:13], v[14:17], v[18:21], v[10:13]
	ds_read_b128 v[18:21], v117 offset:4624
	ds_read_b128 v[34:37], v117 offset:4688
	s_waitcnt lgkmcnt(1)
	v_mfma_f32_16x16x32_f16 v[2:5], v[14:17], v[18:21], v[2:5]
	ds_read_b128 v[14:17], v38 offset:61328
	ds_read_b128 v[18:21], v98 offset:4752
	v_mfma_f32_16x16x32_f16 v[6:9], v[22:25], v[26:29], v[6:9]
	v_mfma_f32_16x16x32_f16 v[10:13], v[22:25], v[30:33], v[10:13]
	s_waitcnt lgkmcnt(2)
	v_mfma_f32_16x16x32_f16 v[22:25], v[22:25], v[34:37], v[2:5]
	s_nop 2
	ds_read_b128 v[2:5], v111 offset:4752
	ds_read_b128 v[26:29], v38 offset:61392
	ds_read_b128 v[30:33], v98 offset:4816
	ds_read_b128 v[34:37], v117 offset:4752
	ds_read_b128 v[38:41], v111 offset:4816
	s_waitcnt lgkmcnt(5)
	v_mfma_f32_16x16x32_f16 v[18:21], v[14:17], v[18:21], v[6:9]
	s_waitcnt lgkmcnt(4)
	v_mfma_f32_16x16x32_f16 v[10:13], v[14:17], v[2:5], v[10:13]
	s_nop 0
	global_load_dwordx4 v[6:9], v[70:71], off nt
	global_load_dwordx4 v[2:5], v[42:43], off nt
	ds_read_b128 v[42:45], v117 offset:4816
	s_waitcnt lgkmcnt(2)
	v_mfma_f32_16x16x32_f16 v[14:17], v[14:17], v[34:37], v[22:25]
	s_nop 2
	v_add_u32_e32 v22, v47, v90
	v_mad_u32_u24 v56, v22, s0, v84
	ds_read_b128 v[22:25], v56 offset:61200
	v_mfma_f32_16x16x32_f16 v[18:21], v[26:29], v[30:33], v[18:21]
	ds_read_b128 v[30:33], v98 offset:8160
	s_waitcnt lgkmcnt(3)
	v_mfma_f32_16x16x32_f16 v[10:13], v[26:29], v[38:41], v[10:13]
	s_waitcnt lgkmcnt(2)
	v_mfma_f32_16x16x32_f16 v[14:17], v[26:29], v[42:45], v[14:17]
	ds_read_b128 v[26:29], v111 offset:8160
	ds_read_b128 v[34:37], v56 offset:61264
	ds_read_b128 v[38:41], v98 offset:8224
	s_waitcnt lgkmcnt(3)
	v_mfma_f32_16x16x32_f16 v[18:21], v[22:25], v[30:33], v[18:21]
	ds_read_b128 v[30:33], v117 offset:8160
	ds_read_b128 v[42:45], v111 offset:8224
	ds_read_b128 v[46:49], v117 offset:8224
	s_waitcnt lgkmcnt(5)
	v_mfma_f32_16x16x32_f16 v[26:29], v[22:25], v[26:29], v[10:13]
	s_waitcnt lgkmcnt(2)
	v_mfma_f32_16x16x32_f16 v[22:25], v[22:25], v[30:33], v[14:17]
	s_nop 2
	global_load_dwordx4 v[14:17], v[50:51], off nt
	global_load_dwordx4 v[10:13], v[52:53], off nt
	ds_read_b128 v[30:33], v56 offset:61328
	v_mfma_f32_16x16x32_f16 v[18:21], v[34:37], v[38:41], v[18:21]
	ds_read_b128 v[38:41], v98 offset:8288
	s_waitcnt lgkmcnt(3)
	v_mfma_f32_16x16x32_f16 v[26:29], v[34:37], v[42:45], v[26:29]
	s_waitcnt lgkmcnt(2)
	v_mfma_f32_16x16x32_f16 v[22:25], v[34:37], v[46:49], v[22:25]
	ds_read_b128 v[34:37], v111 offset:8288
	ds_read_b128 v[42:45], v56 offset:61392
	ds_read_b128 v[46:49], v98 offset:8352
	v_add_co_u32_e32 v56, vcc, 0xa00000, v70
	s_waitcnt lgkmcnt(3)
	v_mfma_f32_16x16x32_f16 v[38:41], v[30:33], v[38:41], v[18:21]
	s_nop 2
	ds_read_b128 v[18:21], v117 offset:8288
	ds_read_b128 v[50:53], v111 offset:8352
	v_addc_co_u32_e32 v57, vcc, 0, v71, vcc
	s_waitcnt lgkmcnt(2)
	v_mfma_f32_16x16x32_f16 v[38:41], v[42:45], v[46:49], v[38:41]
	v_add_u32_e32 v46, v58, v90
	v_mad_u32_u24 v80, v46, s0, v84
	v_add_co_u32_e32 v76, vcc, 0xc00000, v70
	v_mfma_f32_16x16x32_f16 v[26:29], v[30:33], v[34:37], v[26:29]
	ds_read_b128 v[34:37], v117 offset:8352
	v_addc_co_u32_e32 v77, vcc, 0, v71, vcc
	s_waitcnt lgkmcnt(2)
	v_mfma_f32_16x16x32_f16 v[30:33], v[30:33], v[18:21], v[22:25]
	s_nop 2
	global_load_dwordx4 v[22:25], v[54:55], off nt
	global_load_dwordx4 v[18:21], v[56:57], off nt
	ds_read_b128 v[46:49], v80 offset:61200
	v_add_co_u32_e32 v78, vcc, 0xe00000, v70
	s_waitcnt lgkmcnt(2)
	v_mfma_f32_16x16x32_f16 v[26:29], v[42:45], v[50:53], v[26:29]
	ds_read_b128 v[50:53], v98 offset:8432
	v_addc_co_u32_e32 v79, vcc, 0, v71, vcc
	s_waitcnt lgkmcnt(2)
	v_mfma_f32_16x16x32_f16 v[30:33], v[42:45], v[34:37], v[30:33]
	ds_read_b128 v[34:37], v111 offset:8432
	ds_read_b128 v[42:45], v80 offset:61264
	ds_read_b128 v[54:57], v98 offset:8496
	v_add_co_u32_e32 v74, vcc, s1, v82
	s_waitcnt lgkmcnt(3)
	v_mfma_f32_16x16x32_f16 v[38:41], v[46:49], v[50:53], v[38:41]
	ds_read_b128 v[50:53], v117 offset:8432
	ds_read_b128 v[58:61], v111 offset:8496
	ds_read_b128 v[70:73], v117 offset:8496
	v_addc_co_u32_e32 v75, vcc, 0, v83, vcc
	s_waitcnt lgkmcnt(5)
	v_mfma_f32_16x16x32_f16 v[66:69], v[46:49], v[34:37], v[26:29]
	global_load_dwordx4 v[34:37], v[76:77], off nt
	s_nop 1
	global_load_dwordx4 v[26:29], v[78:79], off nt
	v_add_co_u32_e32 v88, vcc, s2, v82
	s_waitcnt lgkmcnt(2)
	v_mfma_f32_16x16x32_f16 v[30:33], v[46:49], v[50:53], v[30:33]
	ds_read_b128 v[46:49], v80 offset:61328
	v_addc_co_u32_e32 v89, vcc, 0, v83, vcc
	v_mfma_f32_16x16x32_f16 v[38:41], v[42:45], v[54:57], v[38:41]
	ds_read_b128 v[54:57], v98 offset:8560
	s_movk_i32 s2, 0xa9
	s_waitcnt lgkmcnt(3)
	v_mfma_f32_16x16x32_f16 v[50:53], v[42:45], v[58:61], v[66:69]
	s_waitcnt lgkmcnt(2)
	v_mfma_f32_16x16x32_f16 v[42:45], v[42:45], v[70:73], v[30:33]
	ds_read_b128 v[58:61], v111 offset:8560
	ds_read_b128 v[66:69], v80 offset:61392
	ds_read_b128 v[70:73], v98 offset:8624
	s_waitcnt lgkmcnt(3)
	v_mfma_f32_16x16x32_f16 v[54:57], v[46:49], v[54:57], v[38:41]
	s_nop 2
	ds_read_b128 v[74:77], v117 offset:8560
	ds_read_b128 v[78:81], v111 offset:8624
	s_waitcnt lgkmcnt(4)
	v_mfma_f32_16x16x32_f16 v[50:53], v[46:49], v[58:61], v[50:53]
	ds_read_b128 v[58:61], v117 offset:8624
	s_waitcnt lgkmcnt(2)
	v_mfma_f32_16x16x32_f16 v[42:45], v[46:49], v[74:77], v[42:45]
	v_mfma_f32_16x16x32_f16 v[46:49], v[66:69], v[70:73], v[54:57]
	ds_read_b128 v[70:73], v98 offset:8704
	s_nop 1
	v_add_u32_e32 v54, v85, v90
	v_mad_u32_u24 v92, v54, s0, v84
	ds_read_b128 v[54:57], v92 offset:61200
	s_waitcnt lgkmcnt(3)
	v_mfma_f32_16x16x32_f16 v[50:53], v[66:69], v[78:81], v[50:53]
	v_add_co_u32_e32 v90, vcc, s3, v82
	s_add_i32 s0, 0, 0x13550
	s_waitcnt lgkmcnt(2)
	v_mfma_f32_16x16x32_f16 v[58:61], v[66:69], v[58:61], v[42:45]
	s_nop 2
	ds_read_b128 v[42:45], v111 offset:8704
	ds_read_b128 v[66:69], v92 offset:61264
	ds_read_b128 v[74:77], v98 offset:8768
	v_addc_co_u32_e32 v91, vcc, 0, v83, vcc
	s_waitcnt lgkmcnt(3)
	v_mfma_f32_16x16x32_f16 v[70:73], v[54:57], v[70:73], v[46:49]
	ds_read_b128 v[78:81], v117 offset:8704
	ds_read_b128 v[82:85], v111 offset:8768
	v_cmp_gt_u32_e64 s[2:3], s2, v64
	v_cmp_eq_u32_e32 vcc, 0, v97
	s_waitcnt lgkmcnt(4)
	v_mfma_f32_16x16x32_f16 v[50:53], v[54:57], v[42:45], v[50:53]
	ds_read_b128 v[88:91], v117 offset:8768
	s_waitcnt lgkmcnt(2)
	v_mfma_f32_16x16x32_f16 v[54:57], v[54:57], v[78:81], v[58:61]
	s_nop 2
	ds_read_b128 v[58:61], v92 offset:61328
	ds_read_b128 v[92:95], v92 offset:61392
	ds_read_b128 v[78:81], v98 offset:8832
	ds_read_b128 v[98:101], v98 offset:8896
	ds_read_b128 v[106:109], v111 offset:8832
	ds_read_b128 v[118:121], v111 offset:8896
	ds_read_b128 v[122:125], v117 offset:8832
	ds_read_b128 v[126:129], v117 offset:8896
	v_mfma_f32_16x16x32_f16 v[102:105], v[66:69], v[74:77], v[70:73]
	s_waitcnt lgkmcnt(9)
	v_mfma_f32_16x16x32_f16 v[50:53], v[66:69], v[82:85], v[50:53]
	s_nop 0
	v_lshlrev_b32_e32 v70, 2, v62
	v_lshl_or_b32 v73, v65, 4, v70
	v_lshl_add_u32 v75, v73, 2, 0
	s_waitcnt lgkmcnt(8)
	v_mfma_f32_16x16x32_f16 v[66:69], v[66:69], v[88:91], v[54:57]
	v_add_u32_e32 v65, 0x13810, v75
	v_min_u32_e32 v72, 0xaf, v64
	v_lshl_add_u32 v70, v63, 2, s0
	s_waitcnt lgkmcnt(5)
	v_mfma_f32_16x16x32_f16 v[54:57], v[58:61], v[78:81], v[102:105]
	v_lshl_add_u32 v71, v110, 2, s0
	v_lshl_add_u32 v72, v72, 2, s0
	ds_read_b32 v65, v65
	ds_read_b32 v79, v70
	ds_read_b32 v78, v71
	ds_read_b32 v77, v72
	s_waitcnt lgkmcnt(7)
	v_mfma_f32_16x16x32_f16 v[80:83], v[58:61], v[106:109], v[50:53]
	s_movk_i32 s0, 0x69
	v_cmp_gt_u32_e64 s[0:1], s0, v63
	s_waitcnt lgkmcnt(5)
	v_mfma_f32_16x16x32_f16 v[58:61], v[58:61], v[122:125], v[66:69]
	v_mfma_f32_16x16x32_f16 v[50:53], v[92:95], v[98:101], v[54:57]
	v_mfma_f32_16x16x32_f16 v[54:57], v[92:95], v[118:121], v[80:83]
	s_waitcnt lgkmcnt(4)
	v_mfma_f32_16x16x32_f16 v[58:61], v[92:95], v[126:129], v[58:61]
	s_waitcnt lgkmcnt(2)
	s_nop 3
	v_or_b32_e32 v69, 1, v73
	v_or_b32_e32 v64, 2, v73
	v_or_b32_e32 v152, 3, v73
	v_lshl_add_u32 v71, v69, 2, 0
	v_lshl_add_u32 v66, v64, 2, 0
	v_lshl_add_u32 v153, v152, 2, 0
	v_add_u32_e32 v160, 0x13810, v71
	v_add_u32_e32 v161, 0x13810, v66
	v_add_u32_e32 v162, 0x13810, v153
	v_mov_b32_e32 v156, 0x13550
	v_lshl_add_u32 v157, v193, 2, v156
	v_lshl_add_u32 v158, v194, 2, v156
	v_lshl_add_u32 v159, v195, 2, v156
	ds_read_b32 v79, v157
	ds_read_b32 v78, v158
	ds_read_b32 v77, v159
	ds_read_b32 v160, v160
	ds_read_b32 v161, v161
	ds_read_b32 v162, v162
	v_mov_b32_e32 v155, 0xff800000
	s_waitcnt lgkmcnt(3)
	v_mul_f32_e32 v164, v50, v79
	v_mul_f32_e32 v165, v54, v78
	v_mul_f32_e32 v166, v58, v77
	v_mul_f32_e32 v164, v65, v164
	v_mul_f32_e32 v165, v65, v165
	v_mul_f32_e32 v166, v65, v166
	v_mul_f32_e32 v167, v51, v79
	v_mul_f32_e32 v168, v55, v78
	v_mul_f32_e32 v169, v59, v77
	v_mul_f32_e32 v170, v52, v79
	v_mul_f32_e32 v171, v56, v78
	v_mul_f32_e32 v172, v60, v77
	v_mul_f32_e32 v173, v53, v79
	v_mul_f32_e32 v174, v57, v78
	v_mul_f32_e32 v175, v61, v77
	s_waitcnt lgkmcnt(0)
	v_mul_f32_e32 v167, v160, v167
	v_mul_f32_e32 v168, v160, v168
	v_mul_f32_e32 v169, v160, v169
	v_mul_f32_e32 v170, v161, v170
	v_mul_f32_e32 v171, v161, v171
	v_mul_f32_e32 v172, v161, v172
	v_mul_f32_e32 v173, v162, v173
	v_mul_f32_e32 v174, v162, v174
	v_mul_f32_e32 v175, v162, v175
	v_cmp_ne_u32_e64 s[8:9], 0, v196
	v_cmp_ne_u32_e64 s[0:1], 0, v197
	v_cmp_ne_u32_e64 s[2:3], 0, v198
	v_cndmask_b32_e64 v164, v155, v164, s[8:9]
	v_cndmask_b32_e64 v167, v155, v167, s[8:9]
	v_cndmask_b32_e64 v170, v155, v170, s[8:9]
	v_cndmask_b32_e64 v173, v155, v173, s[8:9]
	v_cndmask_b32_e64 v165, v155, v165, s[0:1]
	v_cndmask_b32_e64 v166, v155, v166, s[2:3]
	v_cndmask_b32_e64 v168, v155, v168, s[0:1]
	v_cndmask_b32_e64 v169, v155, v169, s[2:3]
	v_cndmask_b32_e64 v171, v155, v171, s[0:1]
	v_cndmask_b32_e64 v172, v155, v172, s[2:3]
	v_cndmask_b32_e64 v174, v155, v174, s[0:1]
	v_cndmask_b32_e64 v175, v155, v175, s[2:3]
	v_max_f32_e32 v176, 0xff800000, v164
	v_max_f32_e32 v177, 0xff800000, v167
	v_max_f32_e32 v178, 0xff800000, v170
	v_max_f32_e32 v179, 0xff800000, v173
	v_max3_f32 v176, v176, v165, v166
	v_max3_f32 v177, v177, v168, v169
	v_max3_f32 v178, v178, v171, v172
	v_max3_f32 v179, v179, v174, v175
	v_max_f32_dpp v176, v176, v176 quad_perm:[1,0,3,2] row_mask:0xf bank_mask:0xf
	v_max_f32_dpp v177, v177, v177 quad_perm:[1,0,3,2] row_mask:0xf bank_mask:0xf
	v_max_f32_dpp v178, v178, v178 quad_perm:[1,0,3,2] row_mask:0xf bank_mask:0xf
	v_max_f32_dpp v179, v179, v179 quad_perm:[1,0,3,2] row_mask:0xf bank_mask:0xf
	v_max_f32_dpp v176, v176, v176 quad_perm:[2,3,0,1] row_mask:0xf bank_mask:0xf
	v_max_f32_dpp v177, v177, v177 quad_perm:[2,3,0,1] row_mask:0xf bank_mask:0xf
	v_max_f32_dpp v178, v178, v178 quad_perm:[2,3,0,1] row_mask:0xf bank_mask:0xf
	v_max_f32_dpp v179, v179, v179 quad_perm:[2,3,0,1] row_mask:0xf bank_mask:0xf
	v_max_f32_dpp v176, v176, v176 row_half_mirror row_mask:0xf bank_mask:0xf
	v_max_f32_dpp v177, v177, v177 row_half_mirror row_mask:0xf bank_mask:0xf
	v_max_f32_dpp v178, v178, v178 row_half_mirror row_mask:0xf bank_mask:0xf
	v_max_f32_dpp v179, v179, v179 row_half_mirror row_mask:0xf bank_mask:0xf
	v_max_f32_dpp v176, v176, v176 row_mirror row_mask:0xf bank_mask:0xf
	v_max_f32_dpp v177, v177, v177 row_mirror row_mask:0xf bank_mask:0xf
	v_max_f32_dpp v178, v178, v178 row_mirror row_mask:0xf bank_mask:0xf
	v_max_f32_dpp v179, v179, v179 row_mirror row_mask:0xf bank_mask:0xf
	v_and_b32_e32 v58, 0x180, v0
	v_add_u32_e32 v58, s6, v58
	v_lshl_add_u32 v58, v73, 2, v58
	s_and_saveexec_b64 s[6:7], vcc
	ds_write_b128 v58, v[176:179]
	s_or_b64 exec, exec, s[6:7]
	v_mov_b32_e32 v76, v164
	v_mov_b32_e32 v74, v165
	v_mov_b32_e32 v72, v166
	v_mov_b32_e32 v70, v167
	v_mov_b32_e32 v68, v168
	v_mov_b32_e32 v67, v169
	v_mov_b32_e32 v65, v170
	v_mov_b32_e32 v59, v171
	v_mov_b32_e32 v56, v172
	v_mov_b32_e32 v53, v173
	v_mov_b32_e32 v52, v174
	v_mov_b32_e32 v50, v175
	v_mov_b32_e32 v54, v152
	v_mov_b32_e32 v55, v153
	v_add_u32_e32 v51, 0x13890, v75
	s_waitcnt lgkmcnt(0)
	s_barrier
	v_add_u32_e32 v152, 0x13890, v75
	ds_read_b128 v[156:159], v152
	ds_read_b128 v[160:163], v152 offset:128
	ds_read_b128 v[164:167], v152 offset:256
	ds_read_b128 v[168:171], v152 offset:384
	v_lshlrev_b32_e32 v51, 3, v62
	v_lshlrev_b32_e32 v60, 8, v73
	v_or_b32_e32 v172, v63, v60
	s_waitcnt lgkmcnt(0)
	v_max_f32_e32 v173, v156, v160
	v_max_f32_e32 v174, v157, v161
	v_max_f32_e32 v175, v158, v162
	v_max_f32_e32 v176, v159, v163
	v_max3_f32 v173, v173, v164, v168
	v_max3_f32 v174, v174, v165, v169
	v_max3_f32 v175, v175, v166, v170
	v_max3_f32 v176, v176, v167, v171
	v_add_f32_e32 v173, 0xbb102de0, v173
	v_add_f32_e32 v174, 0xbb102de0, v174
	v_add_f32_e32 v175, 0xbb102de0, v175
	v_add_f32_e32 v176, 0xbb102de0, v176
	v_cmp_ge_f32_e64 s[90:91], v76, v173
	v_cmp_ge_f32_e64 s[92:93], v74, v173
	v_cmp_ge_f32_e64 s[94:95], v72, v173
	v_cmp_ge_f32_e64 s[96:97], v70, v174
	v_cmp_ge_f32_e64 s[98:99], v68, v174
	v_cmp_ge_f32_e64 s[60:61], v67, v174
	v_cmp_ge_f32_e64 s[62:63], v65, v175
	v_cmp_ge_f32_e64 s[88:89], v59, v175
	v_cmp_ge_f32_e64 s[6:7], v56, v175
	v_cmp_ge_f32_e64 s[8:9], v53, v176
	v_cmp_ge_f32_e64 s[2:3], v52, v176
	v_cmp_ge_f32_e64 s[80:81], v50, v176
	s_bcnt1_i32_b64 s13, s[90:91]
	s_bcnt1_i32_b64 s1, s[92:93]
	s_add_u32 s13, s13, s1
	s_bcnt1_i32_b64 s1, s[94:95]
	s_add_u32 s13, s13, s1
	s_bcnt1_i32_b64 s1, s[96:97]
	s_add_u32 s13, s13, s1
	s_bcnt1_i32_b64 s1, s[98:99]
	s_add_u32 s13, s13, s1
	s_bcnt1_i32_b64 s1, s[60:61]
	s_add_u32 s13, s13, s1
	s_bcnt1_i32_b64 s1, s[62:63]
	s_add_u32 s13, s13, s1
	s_bcnt1_i32_b64 s1, s[88:89]
	s_add_u32 s13, s13, s1
	s_bcnt1_i32_b64 s1, s[6:7]
	s_add_u32 s13, s13, s1
	s_bcnt1_i32_b64 s1, s[8:9]
	s_add_u32 s13, s13, s1
	s_bcnt1_i32_b64 s1, s[2:3]
	s_add_u32 s13, s13, s1
	s_bcnt1_i32_b64 s1, s[80:81]
	s_add_u32 s13, s13, s1
	s_cmp_eq_u32 s13, 0
	s_cbranch_scc1 .Lmy_list_done
	v_mov_b32_e32 v177, 0x13d90
	v_mov_b32_e32 v178, s13
	s_mov_b64 exec, 1
	ds_add_rtn_u32 v179, v177, v178
	s_mov_b64 exec, -1
	s_waitcnt lgkmcnt(0)
	v_readfirstlane_b32 s0, v179
	s_and_saveexec_b64 s[82:83], s[90:91]
	s_cbranch_execz .Lmy_list_skip0
	v_mbcnt_lo_u32_b32 v180, s90, 0
	v_mbcnt_hi_u32_b32 v180, s91, v180
	v_add_u32_e32 v181, 0x0, v60
	v_or_b32_e32 v181, v181, v193
	v_add_lshl_u32 v180, v180, s0, 1
	ds_write_b16 v180, v181
	s_bcnt1_i32_b64 s1, s[90:91]
	s_add_u32 s0, s0, s1
